# strategy: de-synchronise workgroup epilogue store bursts - phase-2 conversion units split 0/2/4/6 before the in_proj GEMM by workgroup (rest after) so GEMM unit phases are staggered
# baseline (speedup 1.0000x reference)
; #define LAS __attribute__((address_space(3)))
; __device__ __forceinline__ void convert_experts(Frame& F, int lo, int hi) {
;     const int gw = F.vcu * 8 + F.wave, NGW = F.G * 8;
;     LAS unsigned char* scr = F.lds + F.wave * 16384;
;     unsigned char* W1t = WSP(F, WS_W1T, unsigned char); unsigned char* W2t = WSP(F, WS_W2T, unsigned char);
;     const float* weg = F.a->in[I_WEG]; const float* weu = F.a->in[I_WEU]; const float* wed = F.a->in[I_WED];
;     const float* wsg = F.a->in[I_WSG]; const float* wsu = F.a->in[I_WSU]; const float* wsd = F.a->in[I_WSD];
;     ...
;     constexpr int NPAIRS = CONV_ITEMS / 2;
;     (void)lo; (void)hi;
;     ...
;     if (gw < NPAIRS) {
;         const int ns = 2 * ((NPAIRS - gw + NGW - 1) / NGW);
;         int sq = 0, r = CONV_RIDX(0);
; __global__ void __launch_bounds__(NTHR, 2) hybrid_fwd(Args args) {
;     ...
;     if (IN(2)) for (int rep = 0; rep < NREP(2); ++rep) {
;         const bool conv_first = (blockIdx.x >> 3) & 1;
;         if (conv_first && rep == 0) { Frame F = make_frame(lds); convert_experts(F, 0, CONV_ITEMS); }
;         { Frame F = make_frame(lds);
;         pg8::DenseSched<512> S; S.init(F.a->ws + WS_A, F.a->ws + WS_WTIN, NTOK, NPROJ, F.G, (int)blockIdx.x, F.tid);
;         EpiBf16T<true> E{WSP(F, WS_B, bf16_t), NPROJ};
;         pg8::gemm_phase<512, EpiBf16T<true>, pg8::DenseSched<512>, true, true>(F.lds, F.tid, S, E); }
;         if (!conv_first && rep == 0) { Frame F = make_frame(lds); convert_experts(F, 0, CONV_ITEMS); }
.LBB0_143:
	s_cmp_lt_i32 s62, 3
	s_cselect_b64 s[6:7], -1, 0
	s_and_b64 s[6:7], s[6:7], s[4:5]
	s_andn2_b64 vcc, exec, s[6:7]
	s_cbranch_vccnz .LBB0_248
	s_bitcmp0_b32 s2, 3
	s_waitcnt lgkmcnt(0)
	s_cselect_b64 s[20:21], -1, 0
	s_ashr_i32 s40, s2, 31
	s_lshr_b32 s3, s40, 29
	s_add_i32 s4, s2, s3
	s_ashr_i32 s3, s4, 3
	s_and_b32 s4, s4, -8
	s_sub_i32 s33, s2, s4
	s_add_u32 s22, s0, 0xd0
	s_addc_u32 s23, s1, 0
	s_and_b64 vcc, exec, s[20:21]
	s_load_dword s8, s[0:1], 0xd0
	s_load_dwordx8 s[72:79], s[0:1], 0x80
	s_load_dwordx4 s[80:83], s[0:1], 0xa0
	s_load_dwordx2 s[84:85], s[0:1], 0xc0
	v_and_b32_e32 v1, 63, v0
	v_lshrrev_b32_e32 v2, 3, v1
	v_and_b32_e32 v3, 7, v1
	v_lshlrev_b32_e32 v4, 4, v3
	v_lshlrev_b32_e32 v5, 4, v2
	v_readfirstlane_b32 s9, v0
	s_waitcnt lgkmcnt(0)
	s_lshr_b32 s9, s9, 6
	s_and_b32 s10, s8, 7
	s_mov_b32 s11, s2
	s_cmp_lg_u32 s10, 0
	s_cbranch_scc1 .Lcv1_vcu
	s_and_b32 s10, s2, 7
	s_lshr_b32 s11, s8, 3
	s_mul_i32 s11, s11, s10
	s_lshr_b32 s10, s2, 3
	s_add_u32 s11, s11, s10
.Lcv1_vcu:
	s_lshl_b32 s11, s11, 3
	s_add_u32 s89, s11, s9
	s_lshl_b32 s71, s8, 3
	s_mul_i32 s10, s71, 18
	s_add_u32 s89, s89, s10
	s_lshr_b32 s10, s11, 3
	s_and_b32 s10, s10, 3
	s_mul_i32 s10, s10, 2
	s_mul_i32 s10, s10, s71
	s_add_u32 s90, s89, s10
	s_min_u32 s90, s90, 49344
	s_mov_b32 s69, s89
	s_add_u32 s86, s84, 0x9180000
	s_addc_u32 s87, s85, 0
	s_add_u32 s84, s84, 0x1100000
	s_addc_u32 s85, s85, 0
	s_cmp_ge_u32 s89, s90
	s_cbranch_scc1 .Lcv1_done
	s_cmp_lt_u32 s69, s90
	s_cbranch_scc0 .Lcv1_dummyA1
	s_lshr_b32 s10, s69, 6
	s_and_b32 s12, s69, 63
	s_mul_hi_u32 s14, s10, 0xaaaaaaab
	s_lshr_b32 s14, s14, 1
	s_mul_i32 s11, s14, 3
	s_sub_u32 s11, s10, s11
	s_cmp_lt_u32 s14, 256
	s_cselect_b32 s10, s14, 0
	s_cselect_b64 s[44:45], -1, 0
	s_lshl_b32 s10, s10, 20
	s_cmp_eq_u32 s11, 2
	s_cbranch_scc1 .Lcv1_downA1
	s_cmp_eq_u32 s11, 0
	s_cselect_b64 s[4:5], s[72:73], s[74:75]
	s_cselect_b64 s[38:39], s[78:79], s[80:81]
	s_mov_b32 s94, 0xc3317218
	s_cselect_b32 s94, 0xc2b8aa3b, s94
	s_cmp_lg_u64 s[44:45], 0
	s_cselect_b64 s[4:5], s[4:5], s[38:39]
	s_lshr_b32 s38, s12, 3
	s_and_b32 s39, s12, 7
	s_lshl_b32 s8, s38, 17
	s_add_u32 s10, s10, s8
	s_lshl_b32 s8, s39, 7
	s_add_u32 s10, s10, s8
	s_add_u32 s4, s4, s10
	s_addc_u32 s5, s5, 0
	s_lshl_b32 s14, s14, 19
	s_lshr_b32 s8, s39, 2
	s_lshl_b32 s8, s8, 18
	s_add_u32 s14, s14, s8
	s_and_b32 s8, s39, 3
	s_lshl_b32 s8, s8, 15
	s_add_u32 s14, s14, s8
	s_lshl_b32 s8, s11, 17
	s_add_u32 s14, s14, s8
	s_lshl_b32 s8, s38, 7
	s_add_u32 s14, s14, s8
	s_add_u32 s92, s84, s14
	s_addc_u32 s93, s85, 0
	s_movk_i32 s25, 0x400
	s_movk_i32 s27, 0x1000
	s_movk_i32 s8, 0x400
	s_movk_i32 s9, 0x4000
	s_branch .Lcv1_goA1

; #define LAS __attribute__((address_space(3)))
; __device__ __forceinline__ void titem_issue(const TItem& t, int lane, LAS unsigned char* buf) {
;     const int nblk = t.N / 32, kb = t.item / nblk, nb = t.item % nblk, k0 = 64 * kb, n0 = 32 * nb;
; #pragma unroll
;     for (int j = 0; j < 8; ++j) { const float* g = t.W + (size_t)(k0 + 8 * j + (lane >> 3)) * t.N + n0 + 4 * ((lane & 7) ^ j);
;         __builtin_amdgcn_global_load_lds((const unsigned*)g, (LAS unsigned*)(buf + j * 1024), 16, 0, 2); }
; }
.Lcv1_goA1:
	s_mov_b32 s95, s94
	v_mad_u32_u24 v6, v2, s9, v4
	global_load_dwordx4 v[32:35], v6, s[4:5] nt
	s_add_u32 s4, s4, s8
	s_addc_u32 s5, s5, 0
	global_load_dwordx4 v[36:39], v6, s[4:5] nt
	s_add_u32 s4, s4, s8
	s_addc_u32 s5, s5, 0
	global_load_dwordx4 v[40:43], v6, s[4:5] nt
	s_add_u32 s4, s4, s8
	s_addc_u32 s5, s5, 0
	global_load_dwordx4 v[44:47], v6, s[4:5] nt
	s_add_u32 s4, s4, s8
	s_addc_u32 s5, s5, 0
	global_load_dwordx4 v[48:51], v6, s[4:5] nt
	s_add_u32 s4, s4, s8
	s_addc_u32 s5, s5, 0
	global_load_dwordx4 v[52:55], v6, s[4:5] nt
	s_add_u32 s4, s4, s8
	s_addc_u32 s5, s5, 0
	global_load_dwordx4 v[56:59], v6, s[4:5] nt
	s_add_u32 s4, s4, s8
	s_addc_u32 s5, s5, 0
	global_load_dwordx4 v[60:63], v6, s[4:5] nt
	s_add_u32 s4, s4, s8
	s_addc_u32 s5, s5, 0
	global_load_dwordx4 v[64:67], v6, s[4:5] nt
	s_add_u32 s4, s4, s8
	s_addc_u32 s5, s5, 0
	global_load_dwordx4 v[68:71], v6, s[4:5] nt
	s_add_u32 s4, s4, s8
	s_addc_u32 s5, s5, 0
	global_load_dwordx4 v[72:75], v6, s[4:5] nt
	s_add_u32 s4, s4, s8
	s_addc_u32 s5, s5, 0
	global_load_dwordx4 v[76:79], v6, s[4:5] nt
	s_add_u32 s4, s4, s8
	s_addc_u32 s5, s5, 0
	global_load_dwordx4 v[80:83], v6, s[4:5] nt
	s_add_u32 s4, s4, s8
	s_addc_u32 s5, s5, 0
	global_load_dwordx4 v[84:87], v6, s[4:5] nt
	s_add_u32 s4, s4, s8
	s_addc_u32 s5, s5, 0
	global_load_dwordx4 v[88:91], v6, s[4:5] nt
	s_add_u32 s4, s4, s8
	s_addc_u32 s5, s5, 0
	global_load_dwordx4 v[92:95], v6, s[4:5] nt
	s_add_u32 s69, s69, s71
	s_cmp_lt_u32 s69, s90
	s_cbranch_scc0 .Lcv1_dummyB2
	s_lshr_b32 s10, s69, 6
	s_and_b32 s12, s69, 63
	s_mul_hi_u32 s14, s10, 0xaaaaaaab
	s_lshr_b32 s14, s14, 1
	s_mul_i32 s11, s14, 3
	s_sub_u32 s11, s10, s11
	s_cmp_lt_u32 s14, 256
	s_cselect_b32 s10, s14, 0
	s_cselect_b64 s[44:45], -1, 0
	s_lshl_b32 s10, s10, 20
	s_cmp_eq_u32 s11, 2
	s_cbranch_scc1 .Lcv1_downB2
	s_cmp_eq_u32 s11, 0
	s_cselect_b64 s[4:5], s[72:73], s[74:75]
	s_cselect_b64 s[38:39], s[78:79], s[80:81]
	s_mov_b32 s98, 0xc3317218
	s_cselect_b32 s98, 0xc2b8aa3b, s98
	s_cmp_lg_u64 s[44:45], 0
	s_cselect_b64 s[4:5], s[4:5], s[38:39]
	s_lshr_b32 s38, s12, 3
	s_and_b32 s39, s12, 7
	s_lshl_b32 s8, s38, 17
	s_add_u32 s10, s10, s8
	s_lshl_b32 s8, s39, 7
	s_add_u32 s10, s10, s8
	s_add_u32 s4, s4, s10
	s_addc_u32 s5, s5, 0
	s_lshl_b32 s14, s14, 19
	s_lshr_b32 s8, s39, 2
	s_lshl_b32 s8, s8, 18
	s_add_u32 s14, s14, s8
	s_and_b32 s8, s39, 3
	s_lshl_b32 s8, s8, 15
	s_add_u32 s14, s14, s8
	s_lshl_b32 s8, s11, 17
	s_add_u32 s14, s14, s8
	s_lshl_b32 s8, s38, 7
	s_add_u32 s14, s14, s8
	s_add_u32 s96, s84, s14
	s_addc_u32 s97, s85, 0
	s_movk_i32 s32, 0x400
	s_movk_i32 s41, 0x1000
	s_movk_i32 s8, 0x400
	s_movk_i32 s9, 0x4000
	s_branch .Lcv1_goB2

; #define LAS __attribute__((address_space(3)))
; __device__ __forceinline__ void titem_issue(const TItem& t, int lane, LAS unsigned char* buf) {
;     const int nblk = t.N / 32, kb = t.item / nblk, nb = t.item % nblk, k0 = 64 * kb, n0 = 32 * nb;
; #pragma unroll
;     for (int j = 0; j < 8; ++j) { const float* g = t.W + (size_t)(k0 + 8 * j + (lane >> 3)) * t.N + n0 + 4 * ((lane & 7) ^ j);
;         __builtin_amdgcn_global_load_lds((const unsigned*)g, (LAS unsigned*)(buf + j * 1024), 16, 0, 2); }
; }
.Lcv1_goB2:
	s_mov_b32 s99, s98
	v_mad_u32_u24 v6, v2, s9, v4
	global_load_dwordx4 v[96:99], v6, s[4:5] nt
	s_add_u32 s4, s4, s8
	s_addc_u32 s5, s5, 0
	global_load_dwordx4 v[100:103], v6, s[4:5] nt
	s_add_u32 s4, s4, s8
	s_addc_u32 s5, s5, 0
	global_load_dwordx4 v[104:107], v6, s[4:5] nt
	s_add_u32 s4, s4, s8
	s_addc_u32 s5, s5, 0
	global_load_dwordx4 v[108:111], v6, s[4:5] nt
	s_add_u32 s4, s4, s8
	s_addc_u32 s5, s5, 0
	global_load_dwordx4 v[112:115], v6, s[4:5] nt
	s_add_u32 s4, s4, s8
	s_addc_u32 s5, s5, 0
	global_load_dwordx4 v[116:119], v6, s[4:5] nt
	s_add_u32 s4, s4, s8
	s_addc_u32 s5, s5, 0
	global_load_dwordx4 v[120:123], v6, s[4:5] nt
	s_add_u32 s4, s4, s8
	s_addc_u32 s5, s5, 0
	global_load_dwordx4 v[124:127], v6, s[4:5] nt
	s_add_u32 s4, s4, s8
	s_addc_u32 s5, s5, 0
	global_load_dwordx4 v[128:131], v6, s[4:5] nt
	s_add_u32 s4, s4, s8
	s_addc_u32 s5, s5, 0
	global_load_dwordx4 v[132:135], v6, s[4:5] nt
	s_add_u32 s4, s4, s8
	s_addc_u32 s5, s5, 0
	global_load_dwordx4 v[136:139], v6, s[4:5] nt
	s_add_u32 s4, s4, s8
	s_addc_u32 s5, s5, 0
	global_load_dwordx4 v[140:143], v6, s[4:5] nt
	s_add_u32 s4, s4, s8
	s_addc_u32 s5, s5, 0
	global_load_dwordx4 v[144:147], v6, s[4:5] nt
	s_add_u32 s4, s4, s8
	s_addc_u32 s5, s5, 0
	global_load_dwordx4 v[148:151], v6, s[4:5] nt
	s_add_u32 s4, s4, s8
	s_addc_u32 s5, s5, 0
	global_load_dwordx4 v[152:155], v6, s[4:5] nt
	s_add_u32 s4, s4, s8
	s_addc_u32 s5, s5, 0
	global_load_dwordx4 v[156:159], v6, s[4:5] nt
	s_add_u32 s69, s69, s71
	s_cmp_lt_u32 s69, s90
	s_cbranch_scc0 .Lcv1_dummyC3
	s_lshr_b32 s10, s69, 6
	s_and_b32 s12, s69, 63
	s_mul_hi_u32 s14, s10, 0xaaaaaaab
	s_lshr_b32 s14, s14, 1
	s_mul_i32 s11, s14, 3
	s_sub_u32 s11, s10, s11
	s_cmp_lt_u32 s14, 256
	s_cselect_b32 s10, s14, 0
	s_cselect_b64 s[44:45], -1, 0
	s_lshl_b32 s10, s10, 20
	s_cmp_eq_u32 s11, 2
	s_cbranch_scc1 .Lcv1_downC3
	s_cmp_eq_u32 s11, 0
	s_cselect_b64 s[4:5], s[72:73], s[74:75]
	s_cselect_b64 s[38:39], s[78:79], s[80:81]
	s_mov_b32 s64, 0xc3317218
	s_cselect_b32 s64, 0xc2b8aa3b, s64
	s_cmp_lg_u64 s[44:45], 0
	s_cselect_b64 s[4:5], s[4:5], s[38:39]
	s_lshr_b32 s38, s12, 3
	s_and_b32 s39, s12, 7
	s_lshl_b32 s8, s38, 17
	s_add_u32 s10, s10, s8
	s_lshl_b32 s8, s39, 7
	s_add_u32 s10, s10, s8
	s_add_u32 s4, s4, s10
	s_addc_u32 s5, s5, 0
	s_lshl_b32 s14, s14, 19
	s_lshr_b32 s8, s39, 2
	s_lshl_b32 s8, s8, 18
	s_add_u32 s14, s14, s8
	s_and_b32 s8, s39, 3
	s_lshl_b32 s8, s8, 15
	s_add_u32 s14, s14, s8
	s_lshl_b32 s8, s11, 17
	s_add_u32 s14, s14, s8
	s_lshl_b32 s8, s38, 7
	s_add_u32 s14, s14, s8
	s_add_u32 s100, s84, s14
	s_addc_u32 s101, s85, 0
	s_movk_i32 s55, 0x400
	s_movk_i32 s58, 0x1000
	s_movk_i32 s8, 0x400
	s_movk_i32 s9, 0x4000
	s_branch .Lcv1_goC3

; #define LAS __attribute__((address_space(3)))
; __device__ __forceinline__ void titem_finish(const TItem& t, int lane, const LAS unsigned char* buf) {
;     const int nblk = t.N / 32, kb = t.item / nblk, nb = t.item % nblk, k0 = 64 * kb, n0 = 32 * nb;
;     const int d0 = t.gmode == 0 ? n0 : ((n0 >> 7) * 256 + (n0 & 127) + (t.gmode == 2 ? 128 : 0));
;     const int c = lane & 7;
;     const LAS float* sb = (const LAS float*)buf;
;     float v[4][8];
;     const float wsc = t.scale;
; #pragma unroll
;     for (int j = 0; j < 4; ++j) { const int n = (lane >> 3) + 8 * j; const LAS float* s = sb + (8 * c) * 32 + 4 * ((n >> 2) ^ c) + (n & 3);
; #pragma unroll
;         for (int q = 0; q < 8; ++q) v[j][q] = s[32 * q] * wsc; }
;     if (t.f8) {
; #pragma unroll
;         for (int j = 0; j < 4; ++j) { const int n = (lane >> 3) + 8 * j;
;             int w0 = __builtin_amdgcn_cvt_pk_fp8_f32(v[j][0], v[j][1], 0, false); w0 = __builtin_amdgcn_cvt_pk_fp8_f32(v[j][2], v[j][3], w0, true);
;             int w1 = __builtin_amdgcn_cvt_pk_fp8_f32(v[j][4], v[j][5], 0, false); w1 = __builtin_amdgcn_cvt_pk_fp8_f32(v[j][6], v[j][7], w1, true);
;             u32x2 o; o.x = (unsigned)w0; o.y = (unsigned)w1;
;             __builtin_nontemporal_store(o, (u32x2*)((unsigned char*)t.WT + (size_t)(d0 + n) * t.K + k0 + 8 * c)); }
; __device__ __forceinline__ void convert_experts(Frame& F, int lo, int hi) {
;     ...
;         for (;;) {
;             const bool more = sq + 1 < ns; const int rn = more ? CONV_RIDX(sq + 1) : r;
;             if (more) { CONV_DESC(rn, tn); titem_issue(tn, F.lane, scr + (p ^ 1) * 8192); }
;             if (!more) asm volatile("s_waitcnt vmcnt(0)" ::: "memory");
;             else if (first) asm volatile("s_waitcnt vmcnt(8)" ::: "memory");
;             else asm volatile("s_waitcnt vmcnt(12)" ::: "memory");
;             titem_finish(tc, F.lane, scr + p * 8192);
;             asm volatile("s_waitcnt lgkmcnt(0)" ::: "memory");
;             if (!more) break;
;             tc = tn; r = rn; ++sq; p ^= 1; first = false;
;         }
.Lcv1_loop:
	s_cmp_ge_u32 s89, s90
	s_cbranch_scc1 .Lcv1_done
	s_waitcnt vmcnt(32)
	v_pk_mul_f32 v[32:33], v[32:33], s[94:95]
	v_pk_mul_f32 v[34:35], v[34:35], s[94:95]
	v_pk_mul_f32 v[36:37], v[36:37], s[94:95]
	v_pk_mul_f32 v[38:39], v[38:39], s[94:95]
	v_pk_mul_f32 v[40:41], v[40:41], s[94:95]
	v_pk_mul_f32 v[42:43], v[42:43], s[94:95]
	v_pk_mul_f32 v[44:45], v[44:45], s[94:95]
	v_pk_mul_f32 v[46:47], v[46:47], s[94:95]
	v_pk_mul_f32 v[48:49], v[48:49], s[94:95]
	v_pk_mul_f32 v[50:51], v[50:51], s[94:95]
	v_pk_mul_f32 v[52:53], v[52:53], s[94:95]
	v_pk_mul_f32 v[54:55], v[54:55], s[94:95]
	v_pk_mul_f32 v[56:57], v[56:57], s[94:95]
	v_pk_mul_f32 v[58:59], v[58:59], s[94:95]
	v_pk_mul_f32 v[60:61], v[60:61], s[94:95]
	v_pk_mul_f32 v[62:63], v[62:63], s[94:95]
	v_pk_mul_f32 v[64:65], v[64:65], s[94:95]
	v_pk_mul_f32 v[66:67], v[66:67], s[94:95]
	v_pk_mul_f32 v[68:69], v[68:69], s[94:95]
	v_pk_mul_f32 v[70:71], v[70:71], s[94:95]
	v_pk_mul_f32 v[72:73], v[72:73], s[94:95]
	v_pk_mul_f32 v[74:75], v[74:75], s[94:95]
	v_pk_mul_f32 v[76:77], v[76:77], s[94:95]
	v_pk_mul_f32 v[78:79], v[78:79], s[94:95]
	v_pk_mul_f32 v[80:81], v[80:81], s[94:95]
	v_pk_mul_f32 v[82:83], v[82:83], s[94:95]
	v_pk_mul_f32 v[84:85], v[84:85], s[94:95]
	v_pk_mul_f32 v[86:87], v[86:87], s[94:95]
	v_pk_mul_f32 v[88:89], v[88:89], s[94:95]
	v_pk_mul_f32 v[90:91], v[90:91], s[94:95]
	v_pk_mul_f32 v[92:93], v[92:93], s[94:95]
	v_pk_mul_f32 v[94:95], v[94:95], s[94:95]
	v_mad_u32_u24 v24, v3, s27, v5
	v_cvt_pk_fp8_f32 v8, v32, v36
	v_cvt_pk_fp8_f32 v9, v48, v52
	v_cvt_pk_fp8_f32 v10, v64, v68
	v_cvt_pk_fp8_f32 v11, v80, v84
	v_cvt_pk_fp8_f32 v12, v33, v37
	v_cvt_pk_fp8_f32 v13, v49, v53
	v_cvt_pk_fp8_f32 v14, v65, v69
	v_cvt_pk_fp8_f32 v15, v81, v85
	v_cvt_pk_fp8_f32 v16, v34, v38
	v_cvt_pk_fp8_f32 v17, v50, v54
	v_cvt_pk_fp8_f32 v18, v66, v70
	v_cvt_pk_fp8_f32 v19, v82, v86
	v_cvt_pk_fp8_f32 v20, v35, v39
	v_cvt_pk_fp8_f32 v21, v51, v55
	v_cvt_pk_fp8_f32 v22, v67, v71
	v_cvt_pk_fp8_f32 v23, v83, v87
	v_add_u32_e32 v25, s25, v24
	v_add_u32_e32 v26, s25, v25
	v_add_u32_e32 v27, s25, v26
	v_cvt_pk_fp8_f32 v8, v40, v44 op_sel:[0,0,1]
	v_cvt_pk_fp8_f32 v9, v56, v60 op_sel:[0,0,1]
	v_cvt_pk_fp8_f32 v10, v72, v76 op_sel:[0,0,1]
	v_cvt_pk_fp8_f32 v11, v88, v92 op_sel:[0,0,1]
	v_cvt_pk_fp8_f32 v12, v41, v45 op_sel:[0,0,1]
	v_cvt_pk_fp8_f32 v13, v57, v61 op_sel:[0,0,1]
	v_cvt_pk_fp8_f32 v14, v73, v77 op_sel:[0,0,1]
	v_cvt_pk_fp8_f32 v15, v89, v93 op_sel:[0,0,1]
	v_cvt_pk_fp8_f32 v16, v42, v46 op_sel:[0,0,1]
	v_cvt_pk_fp8_f32 v17, v58, v62 op_sel:[0,0,1]
	v_cvt_pk_fp8_f32 v18, v74, v78 op_sel:[0,0,1]
	v_cvt_pk_fp8_f32 v19, v90, v94 op_sel:[0,0,1]
	v_cvt_pk_fp8_f32 v20, v43, v47 op_sel:[0,0,1]
	v_cvt_pk_fp8_f32 v21, v59, v63 op_sel:[0,0,1]
	v_cvt_pk_fp8_f32 v22, v75, v79 op_sel:[0,0,1]
	v_cvt_pk_fp8_f32 v23, v91, v95 op_sel:[0,0,1]
	global_store_dwordx4 v24, v[8:11], s[92:93] nt
	global_store_dwordx4 v25, v[12:15], s[92:93] nt
	global_store_dwordx4 v26, v[16:19], s[92:93] nt
	global_store_dwordx4 v27, v[20:23], s[92:93] nt
	s_add_u32 s89, s89, s71
	s_cmp_lt_u32 s69, s90
	s_cbranch_scc0 .Lcv1_dummyA4
	s_lshr_b32 s10, s69, 6
	s_and_b32 s12, s69, 63
	s_mul_hi_u32 s14, s10, 0xaaaaaaab
	s_lshr_b32 s14, s14, 1
	s_mul_i32 s11, s14, 3
	s_sub_u32 s11, s10, s11
	s_cmp_lt_u32 s14, 256
	s_cselect_b32 s10, s14, 0
	s_cselect_b64 s[44:45], -1, 0
	s_lshl_b32 s10, s10, 20
	s_cmp_eq_u32 s11, 2
	s_cbranch_scc1 .Lcv1_downA4
	s_cmp_eq_u32 s11, 0
	s_cselect_b64 s[4:5], s[72:73], s[74:75]
	s_cselect_b64 s[38:39], s[78:79], s[80:81]
	s_mov_b32 s94, 0xc3317218
	s_cselect_b32 s94, 0xc2b8aa3b, s94
	s_cmp_lg_u64 s[44:45], 0
	s_cselect_b64 s[4:5], s[4:5], s[38:39]
	s_lshr_b32 s38, s12, 3
	s_and_b32 s39, s12, 7
	s_lshl_b32 s8, s38, 17
	s_add_u32 s10, s10, s8
	s_lshl_b32 s8, s39, 7
	s_add_u32 s10, s10, s8
	s_add_u32 s4, s4, s10
	s_addc_u32 s5, s5, 0
	s_lshl_b32 s14, s14, 19
	s_lshr_b32 s8, s39, 2
	s_lshl_b32 s8, s8, 18
	s_add_u32 s14, s14, s8
	s_and_b32 s8, s39, 3
	s_lshl_b32 s8, s8, 15
	s_add_u32 s14, s14, s8
	s_lshl_b32 s8, s11, 17
	s_add_u32 s14, s14, s8
	s_lshl_b32 s8, s38, 7
	s_add_u32 s14, s14, s8
	s_add_u32 s92, s84, s14
	s_addc_u32 s93, s85, 0
	s_movk_i32 s25, 0x400
	s_movk_i32 s27, 0x1000
	s_movk_i32 s8, 0x400
	s_movk_i32 s9, 0x4000
	s_branch .Lcv1_goA4

; #define LAS __attribute__((address_space(3)))
; __device__ __forceinline__ void titem_finish(const TItem& t, int lane, const LAS unsigned char* buf) {
;     const int nblk = t.N / 32, kb = t.item / nblk, nb = t.item % nblk, k0 = 64 * kb, n0 = 32 * nb;
;     const int d0 = t.gmode == 0 ? n0 : ((n0 >> 7) * 256 + (n0 & 127) + (t.gmode == 2 ? 128 : 0));
;     const int c = lane & 7;
;     const LAS float* sb = (const LAS float*)buf;
;     float v[4][8];
;     const float wsc = t.scale;
; #pragma unroll
;     for (int j = 0; j < 4; ++j) { const int n = (lane >> 3) + 8 * j; const LAS float* s = sb + (8 * c) * 32 + 4 * ((n >> 2) ^ c) + (n & 3);
; #pragma unroll
;         for (int q = 0; q < 8; ++q) v[j][q] = s[32 * q] * wsc; }
;     if (t.f8) {
; #pragma unroll
;         for (int j = 0; j < 4; ++j) { const int n = (lane >> 3) + 8 * j;
;             int w0 = __builtin_amdgcn_cvt_pk_fp8_f32(v[j][0], v[j][1], 0, false); w0 = __builtin_amdgcn_cvt_pk_fp8_f32(v[j][2], v[j][3], w0, true);
;             int w1 = __builtin_amdgcn_cvt_pk_fp8_f32(v[j][4], v[j][5], 0, false); w1 = __builtin_amdgcn_cvt_pk_fp8_f32(v[j][6], v[j][7], w1, true);
;             u32x2 o; o.x = (unsigned)w0; o.y = (unsigned)w1;
;             __builtin_nontemporal_store(o, (u32x2*)((unsigned char*)t.WT + (size_t)(d0 + n) * t.K + k0 + 8 * c)); }
; __device__ __forceinline__ void convert_experts(Frame& F, int lo, int hi) {
;     ...
;         for (;;) {
;             const bool more = sq + 1 < ns; const int rn = more ? CONV_RIDX(sq + 1) : r;
;             if (more) { CONV_DESC(rn, tn); titem_issue(tn, F.lane, scr + (p ^ 1) * 8192); }
;             if (!more) asm volatile("s_waitcnt vmcnt(0)" ::: "memory");
;             else if (first) asm volatile("s_waitcnt vmcnt(8)" ::: "memory");
;             else asm volatile("s_waitcnt vmcnt(12)" ::: "memory");
;             titem_finish(tc, F.lane, scr + p * 8192);
;             asm volatile("s_waitcnt lgkmcnt(0)" ::: "memory");
;             if (!more) break;
;             tc = tn; r = rn; ++sq; p ^= 1; first = false;
;         }
.Lcv1_goA4:
	s_mov_b32 s95, s94
	v_mad_u32_u24 v6, v2, s9, v4
	global_load_dwordx4 v[32:35], v6, s[4:5] nt
	s_add_u32 s4, s4, s8
	s_addc_u32 s5, s5, 0
	global_load_dwordx4 v[36:39], v6, s[4:5] nt
	s_add_u32 s4, s4, s8
	s_addc_u32 s5, s5, 0
	global_load_dwordx4 v[40:43], v6, s[4:5] nt
	s_add_u32 s4, s4, s8
	s_addc_u32 s5, s5, 0
	global_load_dwordx4 v[44:47], v6, s[4:5] nt
	s_add_u32 s4, s4, s8
	s_addc_u32 s5, s5, 0
	global_load_dwordx4 v[48:51], v6, s[4:5] nt
	s_add_u32 s4, s4, s8
	s_addc_u32 s5, s5, 0
	global_load_dwordx4 v[52:55], v6, s[4:5] nt
	s_add_u32 s4, s4, s8
	s_addc_u32 s5, s5, 0
	global_load_dwordx4 v[56:59], v6, s[4:5] nt
	s_add_u32 s4, s4, s8
	s_addc_u32 s5, s5, 0
	global_load_dwordx4 v[60:63], v6, s[4:5] nt
	s_add_u32 s4, s4, s8
	s_addc_u32 s5, s5, 0
	global_load_dwordx4 v[64:67], v6, s[4:5] nt
	s_add_u32 s4, s4, s8
	s_addc_u32 s5, s5, 0
	global_load_dwordx4 v[68:71], v6, s[4:5] nt
	s_add_u32 s4, s4, s8
	s_addc_u32 s5, s5, 0
	global_load_dwordx4 v[72:75], v6, s[4:5] nt
	s_add_u32 s4, s4, s8
	s_addc_u32 s5, s5, 0
	global_load_dwordx4 v[76:79], v6, s[4:5] nt
	s_add_u32 s4, s4, s8
	s_addc_u32 s5, s5, 0
	global_load_dwordx4 v[80:83], v6, s[4:5] nt
	s_add_u32 s4, s4, s8
	s_addc_u32 s5, s5, 0
	global_load_dwordx4 v[84:87], v6, s[4:5] nt
	s_add_u32 s4, s4, s8
	s_addc_u32 s5, s5, 0
	global_load_dwordx4 v[88:91], v6, s[4:5] nt
	s_add_u32 s4, s4, s8
	s_addc_u32 s5, s5, 0
	global_load_dwordx4 v[92:95], v6, s[4:5] nt
	s_add_u32 s69, s69, s71
	s_cmp_ge_u32 s89, s90
	s_cbranch_scc1 .Lcv1_done
	s_waitcnt vmcnt(36)
	v_pk_mul_f32 v[96:97], v[96:97], s[98:99]
	v_pk_mul_f32 v[98:99], v[98:99], s[98:99]
	v_pk_mul_f32 v[100:101], v[100:101], s[98:99]
	v_pk_mul_f32 v[102:103], v[102:103], s[98:99]
	v_pk_mul_f32 v[104:105], v[104:105], s[98:99]
	v_pk_mul_f32 v[106:107], v[106:107], s[98:99]
	v_pk_mul_f32 v[108:109], v[108:109], s[98:99]
	v_pk_mul_f32 v[110:111], v[110:111], s[98:99]
	v_pk_mul_f32 v[112:113], v[112:113], s[98:99]
	v_pk_mul_f32 v[114:115], v[114:115], s[98:99]
	v_pk_mul_f32 v[116:117], v[116:117], s[98:99]
	v_pk_mul_f32 v[118:119], v[118:119], s[98:99]
	v_pk_mul_f32 v[120:121], v[120:121], s[98:99]
	v_pk_mul_f32 v[122:123], v[122:123], s[98:99]
	v_pk_mul_f32 v[124:125], v[124:125], s[98:99]
	v_pk_mul_f32 v[126:127], v[126:127], s[98:99]
	v_pk_mul_f32 v[128:129], v[128:129], s[98:99]
	v_pk_mul_f32 v[130:131], v[130:131], s[98:99]
	v_pk_mul_f32 v[132:133], v[132:133], s[98:99]
	v_pk_mul_f32 v[134:135], v[134:135], s[98:99]
	v_pk_mul_f32 v[136:137], v[136:137], s[98:99]
	v_pk_mul_f32 v[138:139], v[138:139], s[98:99]
	v_pk_mul_f32 v[140:141], v[140:141], s[98:99]
	v_pk_mul_f32 v[142:143], v[142:143], s[98:99]
	v_pk_mul_f32 v[144:145], v[144:145], s[98:99]
	v_pk_mul_f32 v[146:147], v[146:147], s[98:99]
	v_pk_mul_f32 v[148:149], v[148:149], s[98:99]
	v_pk_mul_f32 v[150:151], v[150:151], s[98:99]
	v_pk_mul_f32 v[152:153], v[152:153], s[98:99]
	v_pk_mul_f32 v[154:155], v[154:155], s[98:99]
	v_pk_mul_f32 v[156:157], v[156:157], s[98:99]
	v_pk_mul_f32 v[158:159], v[158:159], s[98:99]
	v_mad_u32_u24 v24, v3, s41, v5
	v_cvt_pk_fp8_f32 v8, v96, v100
	v_cvt_pk_fp8_f32 v9, v112, v116
	v_cvt_pk_fp8_f32 v10, v128, v132
	v_cvt_pk_fp8_f32 v11, v144, v148
	v_cvt_pk_fp8_f32 v12, v97, v101
	v_cvt_pk_fp8_f32 v13, v113, v117
	v_cvt_pk_fp8_f32 v14, v129, v133
	v_cvt_pk_fp8_f32 v15, v145, v149
	v_cvt_pk_fp8_f32 v16, v98, v102
	v_cvt_pk_fp8_f32 v17, v114, v118
	v_cvt_pk_fp8_f32 v18, v130, v134
	v_cvt_pk_fp8_f32 v19, v146, v150
	v_cvt_pk_fp8_f32 v20, v99, v103
	v_cvt_pk_fp8_f32 v21, v115, v119
	v_cvt_pk_fp8_f32 v22, v131, v135
	v_cvt_pk_fp8_f32 v23, v147, v151
	v_add_u32_e32 v25, s32, v24
	v_add_u32_e32 v26, s32, v25
	v_add_u32_e32 v27, s32, v26
	v_cvt_pk_fp8_f32 v8, v104, v108 op_sel:[0,0,1]
	v_cvt_pk_fp8_f32 v9, v120, v124 op_sel:[0,0,1]
	v_cvt_pk_fp8_f32 v10, v136, v140 op_sel:[0,0,1]
	v_cvt_pk_fp8_f32 v11, v152, v156 op_sel:[0,0,1]
	v_cvt_pk_fp8_f32 v12, v105, v109 op_sel:[0,0,1]
	v_cvt_pk_fp8_f32 v13, v121, v125 op_sel:[0,0,1]
	v_cvt_pk_fp8_f32 v14, v137, v141 op_sel:[0,0,1]
	v_cvt_pk_fp8_f32 v15, v153, v157 op_sel:[0,0,1]
	v_cvt_pk_fp8_f32 v16, v106, v110 op_sel:[0,0,1]
	v_cvt_pk_fp8_f32 v17, v122, v126 op_sel:[0,0,1]
	v_cvt_pk_fp8_f32 v18, v138, v142 op_sel:[0,0,1]
	v_cvt_pk_fp8_f32 v19, v154, v158 op_sel:[0,0,1]
	v_cvt_pk_fp8_f32 v20, v107, v111 op_sel:[0,0,1]
	v_cvt_pk_fp8_f32 v21, v123, v127 op_sel:[0,0,1]
	v_cvt_pk_fp8_f32 v22, v139, v143 op_sel:[0,0,1]
	v_cvt_pk_fp8_f32 v23, v155, v159 op_sel:[0,0,1]
	global_store_dwordx4 v24, v[8:11], s[96:97] nt
	global_store_dwordx4 v25, v[12:15], s[96:97] nt
	global_store_dwordx4 v26, v[16:19], s[96:97] nt
	global_store_dwordx4 v27, v[20:23], s[96:97] nt
	s_add_u32 s89, s89, s71
	s_cmp_lt_u32 s69, s90
	s_cbranch_scc0 .Lcv1_dummyB5
	s_lshr_b32 s10, s69, 6
	s_and_b32 s12, s69, 63
	s_mul_hi_u32 s14, s10, 0xaaaaaaab
	s_lshr_b32 s14, s14, 1
	s_mul_i32 s11, s14, 3
	s_sub_u32 s11, s10, s11
	s_cmp_lt_u32 s14, 256
	s_cselect_b32 s10, s14, 0
	s_cselect_b64 s[44:45], -1, 0
	s_lshl_b32 s10, s10, 20
	s_cmp_eq_u32 s11, 2
	s_cbranch_scc1 .Lcv1_downB5
	s_cmp_eq_u32 s11, 0
	s_cselect_b64 s[4:5], s[72:73], s[74:75]
	s_cselect_b64 s[38:39], s[78:79], s[80:81]
	s_mov_b32 s98, 0xc3317218
	s_cselect_b32 s98, 0xc2b8aa3b, s98
	s_cmp_lg_u64 s[44:45], 0
	s_cselect_b64 s[4:5], s[4:5], s[38:39]
	s_lshr_b32 s38, s12, 3
	s_and_b32 s39, s12, 7
	s_lshl_b32 s8, s38, 17
	s_add_u32 s10, s10, s8
	s_lshl_b32 s8, s39, 7
	s_add_u32 s10, s10, s8
	s_add_u32 s4, s4, s10
	s_addc_u32 s5, s5, 0
	s_lshl_b32 s14, s14, 19
	s_lshr_b32 s8, s39, 2
	s_lshl_b32 s8, s8, 18
	s_add_u32 s14, s14, s8
	s_and_b32 s8, s39, 3
	s_lshl_b32 s8, s8, 15
	s_add_u32 s14, s14, s8
	s_lshl_b32 s8, s11, 17
	s_add_u32 s14, s14, s8
	s_lshl_b32 s8, s38, 7
	s_add_u32 s14, s14, s8
	s_add_u32 s96, s84, s14
	s_addc_u32 s97, s85, 0
	s_movk_i32 s32, 0x400
	s_movk_i32 s41, 0x1000
	s_movk_i32 s8, 0x400
	s_movk_i32 s9, 0x4000
	s_branch .Lcv1_goB5

; #define LAS __attribute__((address_space(3)))
; __device__ __forceinline__ void titem_finish(const TItem& t, int lane, const LAS unsigned char* buf) {
;     const int nblk = t.N / 32, kb = t.item / nblk, nb = t.item % nblk, k0 = 64 * kb, n0 = 32 * nb;
;     const int d0 = t.gmode == 0 ? n0 : ((n0 >> 7) * 256 + (n0 & 127) + (t.gmode == 2 ? 128 : 0));
;     const int c = lane & 7;
;     const LAS float* sb = (const LAS float*)buf;
;     float v[4][8];
;     const float wsc = t.scale;
; #pragma unroll
;     for (int j = 0; j < 4; ++j) { const int n = (lane >> 3) + 8 * j; const LAS float* s = sb + (8 * c) * 32 + 4 * ((n >> 2) ^ c) + (n & 3);
; #pragma unroll
;         for (int q = 0; q < 8; ++q) v[j][q] = s[32 * q] * wsc; }
;     if (t.f8) {
; #pragma unroll
;         for (int j = 0; j < 4; ++j) { const int n = (lane >> 3) + 8 * j;
;             int w0 = __builtin_amdgcn_cvt_pk_fp8_f32(v[j][0], v[j][1], 0, false); w0 = __builtin_amdgcn_cvt_pk_fp8_f32(v[j][2], v[j][3], w0, true);
;             int w1 = __builtin_amdgcn_cvt_pk_fp8_f32(v[j][4], v[j][5], 0, false); w1 = __builtin_amdgcn_cvt_pk_fp8_f32(v[j][6], v[j][7], w1, true);
;             u32x2 o; o.x = (unsigned)w0; o.y = (unsigned)w1;
;             __builtin_nontemporal_store(o, (u32x2*)((unsigned char*)t.WT + (size_t)(d0 + n) * t.K + k0 + 8 * c)); }
; __device__ __forceinline__ void convert_experts(Frame& F, int lo, int hi) {
;     ...
;         for (;;) {
;             const bool more = sq + 1 < ns; const int rn = more ? CONV_RIDX(sq + 1) : r;
;             if (more) { CONV_DESC(rn, tn); titem_issue(tn, F.lane, scr + (p ^ 1) * 8192); }
;             if (!more) asm volatile("s_waitcnt vmcnt(0)" ::: "memory");
;             else if (first) asm volatile("s_waitcnt vmcnt(8)" ::: "memory");
;             else asm volatile("s_waitcnt vmcnt(12)" ::: "memory");
;             titem_finish(tc, F.lane, scr + p * 8192);
;             asm volatile("s_waitcnt lgkmcnt(0)" ::: "memory");
;             if (!more) break;
;             tc = tn; r = rn; ++sq; p ^= 1; first = false;
;         }
.Lcv1_goB5:
	s_mov_b32 s99, s98
	v_mad_u32_u24 v6, v2, s9, v4
	global_load_dwordx4 v[96:99], v6, s[4:5] nt
	s_add_u32 s4, s4, s8
	s_addc_u32 s5, s5, 0
	global_load_dwordx4 v[100:103], v6, s[4:5] nt
	s_add_u32 s4, s4, s8
	s_addc_u32 s5, s5, 0
	global_load_dwordx4 v[104:107], v6, s[4:5] nt
	s_add_u32 s4, s4, s8
	s_addc_u32 s5, s5, 0
	global_load_dwordx4 v[108:111], v6, s[4:5] nt
	s_add_u32 s4, s4, s8
	s_addc_u32 s5, s5, 0
	global_load_dwordx4 v[112:115], v6, s[4:5] nt
	s_add_u32 s4, s4, s8
	s_addc_u32 s5, s5, 0
	global_load_dwordx4 v[116:119], v6, s[4:5] nt
	s_add_u32 s4, s4, s8
	s_addc_u32 s5, s5, 0
	global_load_dwordx4 v[120:123], v6, s[4:5] nt
	s_add_u32 s4, s4, s8
	s_addc_u32 s5, s5, 0
	global_load_dwordx4 v[124:127], v6, s[4:5] nt
	s_add_u32 s4, s4, s8
	s_addc_u32 s5, s5, 0
	global_load_dwordx4 v[128:131], v6, s[4:5] nt
	s_add_u32 s4, s4, s8
	s_addc_u32 s5, s5, 0
	global_load_dwordx4 v[132:135], v6, s[4:5] nt
	s_add_u32 s4, s4, s8
	s_addc_u32 s5, s5, 0
	global_load_dwordx4 v[136:139], v6, s[4:5] nt
	s_add_u32 s4, s4, s8
	s_addc_u32 s5, s5, 0
	global_load_dwordx4 v[140:143], v6, s[4:5] nt
	s_add_u32 s4, s4, s8
	s_addc_u32 s5, s5, 0
	global_load_dwordx4 v[144:147], v6, s[4:5] nt
	s_add_u32 s4, s4, s8
	s_addc_u32 s5, s5, 0
	global_load_dwordx4 v[148:151], v6, s[4:5] nt
	s_add_u32 s4, s4, s8
	s_addc_u32 s5, s5, 0
	global_load_dwordx4 v[152:155], v6, s[4:5] nt
	s_add_u32 s4, s4, s8
	s_addc_u32 s5, s5, 0
	global_load_dwordx4 v[156:159], v6, s[4:5] nt
	s_add_u32 s69, s69, s71
	s_cmp_ge_u32 s89, s90
	s_cbranch_scc1 .Lcv1_done
	s_waitcnt vmcnt(40)
	v_pk_mul_f32 v[164:165], v[164:165], s[64:65]
	v_pk_mul_f32 v[166:167], v[166:167], s[64:65]
	v_pk_mul_f32 v[168:169], v[168:169], s[64:65]
	v_pk_mul_f32 v[170:171], v[170:171], s[64:65]
	v_pk_mul_f32 v[172:173], v[172:173], s[64:65]
	v_pk_mul_f32 v[174:175], v[174:175], s[64:65]
	v_pk_mul_f32 v[176:177], v[176:177], s[64:65]
	v_pk_mul_f32 v[178:179], v[178:179], s[64:65]
	v_pk_mul_f32 v[180:181], v[180:181], s[64:65]
	v_pk_mul_f32 v[182:183], v[182:183], s[64:65]
	v_pk_mul_f32 v[184:185], v[184:185], s[64:65]
	v_pk_mul_f32 v[186:187], v[186:187], s[64:65]
	v_pk_mul_f32 v[188:189], v[188:189], s[64:65]
	v_pk_mul_f32 v[190:191], v[190:191], s[64:65]
	v_pk_mul_f32 v[192:193], v[192:193], s[64:65]
	v_pk_mul_f32 v[194:195], v[194:195], s[64:65]
	v_pk_mul_f32 v[196:197], v[196:197], s[64:65]
	v_pk_mul_f32 v[198:199], v[198:199], s[64:65]
	v_pk_mul_f32 v[200:201], v[200:201], s[64:65]
	v_pk_mul_f32 v[202:203], v[202:203], s[64:65]
	v_pk_mul_f32 v[204:205], v[204:205], s[64:65]
	v_pk_mul_f32 v[206:207], v[206:207], s[64:65]
	v_pk_mul_f32 v[208:209], v[208:209], s[64:65]
	v_pk_mul_f32 v[210:211], v[210:211], s[64:65]
	v_pk_mul_f32 v[212:213], v[212:213], s[64:65]
	v_pk_mul_f32 v[214:215], v[214:215], s[64:65]
	v_pk_mul_f32 v[216:217], v[216:217], s[64:65]
	v_pk_mul_f32 v[218:219], v[218:219], s[64:65]
	v_pk_mul_f32 v[220:221], v[220:221], s[64:65]
	v_pk_mul_f32 v[222:223], v[222:223], s[64:65]
	v_pk_mul_f32 v[224:225], v[224:225], s[64:65]
	v_pk_mul_f32 v[226:227], v[226:227], s[64:65]
	v_mad_u32_u24 v24, v3, s58, v5
	v_cvt_pk_fp8_f32 v8, v164, v168
	v_cvt_pk_fp8_f32 v9, v180, v184
	v_cvt_pk_fp8_f32 v10, v196, v200
	v_cvt_pk_fp8_f32 v11, v212, v216
	v_cvt_pk_fp8_f32 v12, v165, v169
	v_cvt_pk_fp8_f32 v13, v181, v185
	v_cvt_pk_fp8_f32 v14, v197, v201
	v_cvt_pk_fp8_f32 v15, v213, v217
	v_cvt_pk_fp8_f32 v16, v166, v170
	v_cvt_pk_fp8_f32 v17, v182, v186
	v_cvt_pk_fp8_f32 v18, v198, v202
	v_cvt_pk_fp8_f32 v19, v214, v218
	v_cvt_pk_fp8_f32 v20, v167, v171
	v_cvt_pk_fp8_f32 v21, v183, v187
	v_cvt_pk_fp8_f32 v22, v199, v203
	v_cvt_pk_fp8_f32 v23, v215, v219
	v_add_u32_e32 v25, s55, v24
	v_add_u32_e32 v26, s55, v25
	v_add_u32_e32 v27, s55, v26
	v_cvt_pk_fp8_f32 v8, v172, v176 op_sel:[0,0,1]
	v_cvt_pk_fp8_f32 v9, v188, v192 op_sel:[0,0,1]
	v_cvt_pk_fp8_f32 v10, v204, v208 op_sel:[0,0,1]
	v_cvt_pk_fp8_f32 v11, v220, v224 op_sel:[0,0,1]
	v_cvt_pk_fp8_f32 v12, v173, v177 op_sel:[0,0,1]
	v_cvt_pk_fp8_f32 v13, v189, v193 op_sel:[0,0,1]
	v_cvt_pk_fp8_f32 v14, v205, v209 op_sel:[0,0,1]
	v_cvt_pk_fp8_f32 v15, v221, v225 op_sel:[0,0,1]
	v_cvt_pk_fp8_f32 v16, v174, v178 op_sel:[0,0,1]
	v_cvt_pk_fp8_f32 v17, v190, v194 op_sel:[0,0,1]
	v_cvt_pk_fp8_f32 v18, v206, v210 op_sel:[0,0,1]
	v_cvt_pk_fp8_f32 v19, v222, v226 op_sel:[0,0,1]
	v_cvt_pk_fp8_f32 v20, v175, v179 op_sel:[0,0,1]
	v_cvt_pk_fp8_f32 v21, v191, v195 op_sel:[0,0,1]
	v_cvt_pk_fp8_f32 v22, v207, v211 op_sel:[0,0,1]
	v_cvt_pk_fp8_f32 v23, v223, v227 op_sel:[0,0,1]
	global_store_dwordx4 v24, v[8:11], s[100:101] nt
	global_store_dwordx4 v25, v[12:15], s[100:101] nt
	global_store_dwordx4 v26, v[16:19], s[100:101] nt
	global_store_dwordx4 v27, v[20:23], s[100:101] nt
	s_add_u32 s89, s89, s71
	s_cmp_lt_u32 s69, s90
	s_cbranch_scc0 .Lcv1_dummyC6
	s_lshr_b32 s10, s69, 6
	s_and_b32 s12, s69, 63
	s_mul_hi_u32 s14, s10, 0xaaaaaaab
	s_lshr_b32 s14, s14, 1
	s_mul_i32 s11, s14, 3
	s_sub_u32 s11, s10, s11
	s_cmp_lt_u32 s14, 256
	s_cselect_b32 s10, s14, 0
	s_cselect_b64 s[44:45], -1, 0
	s_lshl_b32 s10, s10, 20
	s_cmp_eq_u32 s11, 2
	s_cbranch_scc1 .Lcv1_downC6
	s_cmp_eq_u32 s11, 0
	s_cselect_b64 s[4:5], s[72:73], s[74:75]
	s_cselect_b64 s[38:39], s[78:79], s[80:81]
	s_mov_b32 s64, 0xc3317218
	s_cselect_b32 s64, 0xc2b8aa3b, s64
	s_cmp_lg_u64 s[44:45], 0
	s_cselect_b64 s[4:5], s[4:5], s[38:39]
	s_lshr_b32 s38, s12, 3
	s_and_b32 s39, s12, 7
	s_lshl_b32 s8, s38, 17
	s_add_u32 s10, s10, s8
	s_lshl_b32 s8, s39, 7
	s_add_u32 s10, s10, s8
	s_add_u32 s4, s4, s10
	s_addc_u32 s5, s5, 0
	s_lshl_b32 s14, s14, 19
	s_lshr_b32 s8, s39, 2
	s_lshl_b32 s8, s8, 18
	s_add_u32 s14, s14, s8
	s_and_b32 s8, s39, 3
	s_lshl_b32 s8, s8, 15
	s_add_u32 s14, s14, s8
	s_lshl_b32 s8, s11, 17
	s_add_u32 s14, s14, s8
	s_lshl_b32 s8, s38, 7
	s_add_u32 s14, s14, s8
	s_add_u32 s100, s84, s14
	s_addc_u32 s101, s85, 0
	s_movk_i32 s55, 0x400
	s_movk_i32 s58, 0x1000
	s_movk_i32 s8, 0x400
	s_movk_i32 s9, 0x4000
	s_branch .Lcv1_goC6

; #define LAS __attribute__((address_space(3)))
; __device__ __forceinline__ void convert_experts(Frame& F, int lo, int hi) {
;     const int gw = F.vcu * 8 + F.wave, NGW = F.G * 8;
;     LAS unsigned char* scr = F.lds + F.wave * 16384;
;     unsigned char* W1t = WSP(F, WS_W1T, unsigned char); unsigned char* W2t = WSP(F, WS_W2T, unsigned char);
;     const float* weg = F.a->in[I_WEG]; const float* weu = F.a->in[I_WEU]; const float* wed = F.a->in[I_WED];
;     const float* wsg = F.a->in[I_WSG]; const float* wsu = F.a->in[I_WSU]; const float* wsd = F.a->in[I_WSD];
;     ...
;     constexpr int NPAIRS = CONV_ITEMS / 2;
;     (void)lo; (void)hi;
;     ...
;     if (gw < NPAIRS) {
;         const int ns = 2 * ((NPAIRS - gw + NGW - 1) / NGW);
;         int sq = 0, r = CONV_RIDX(0);
.LBB0_203:
	s_andn2_b64 vcc, exec, s[20:21]
	s_load_dword s8, s[0:1], 0xd0
	s_load_dwordx8 s[72:79], s[0:1], 0x80
	s_load_dwordx4 s[80:83], s[0:1], 0xa0
	s_load_dwordx2 s[84:85], s[0:1], 0xc0
	v_and_b32_e32 v1, 63, v0
	v_lshrrev_b32_e32 v2, 3, v1
	v_and_b32_e32 v3, 7, v1
	v_lshlrev_b32_e32 v4, 4, v3
	v_lshlrev_b32_e32 v5, 4, v2
	v_readfirstlane_b32 s9, v0
	s_waitcnt lgkmcnt(0)
	s_lshr_b32 s9, s9, 6
	s_and_b32 s10, s8, 7
	s_mov_b32 s11, s2
	s_cmp_lg_u32 s10, 0
	s_cbranch_scc1 .Lcv2_vcu
	s_and_b32 s10, s2, 7
	s_lshr_b32 s11, s8, 3
	s_mul_i32 s11, s11, s10
	s_lshr_b32 s10, s2, 3
	s_add_u32 s11, s11, s10
.Lcv2_vcu:
	s_lshl_b32 s11, s11, 3
	s_add_u32 s89, s11, s9
	s_lshl_b32 s71, s8, 3
	s_mul_i32 s10, s71, 18
	s_add_u32 s89, s89, s10
	s_lshr_b32 s10, s11, 3
	s_and_b32 s10, s10, 3
	s_mul_i32 s10, s10, 2
	s_mul_i32 s10, s10, s71
	s_add_u32 s89, s89, s10
	s_mov_b32 s90, 49344
	s_mov_b32 s69, s89
	s_add_u32 s86, s84, 0x9180000
	s_addc_u32 s87, s85, 0
	s_add_u32 s84, s84, 0x1100000
	s_addc_u32 s85, s85, 0
	s_cmp_ge_u32 s89, s90
	s_cbranch_scc1 .Lcv2_done
	s_cmp_lt_u32 s69, s90
	s_cbranch_scc0 .Lcv2_dummyA1
	s_lshr_b32 s10, s69, 6
	s_and_b32 s12, s69, 63
	s_mul_hi_u32 s14, s10, 0xaaaaaaab
	s_lshr_b32 s14, s14, 1
	s_mul_i32 s11, s14, 3
	s_sub_u32 s11, s10, s11
	s_cmp_lt_u32 s14, 256
	s_cselect_b32 s10, s14, 0
	s_cselect_b64 s[44:45], -1, 0
	s_lshl_b32 s10, s10, 20
	s_cmp_eq_u32 s11, 2
	s_cbranch_scc1 .Lcv2_downA1
	s_cmp_eq_u32 s11, 0
	s_cselect_b64 s[4:5], s[72:73], s[74:75]
	s_cselect_b64 s[38:39], s[78:79], s[80:81]
	s_mov_b32 s94, 0xc3317218
	s_cselect_b32 s94, 0xc2b8aa3b, s94
	s_cmp_lg_u64 s[44:45], 0
	s_cselect_b64 s[4:5], s[4:5], s[38:39]
	s_lshr_b32 s38, s12, 3
	s_and_b32 s39, s12, 7
	s_lshl_b32 s8, s38, 17
	s_add_u32 s10, s10, s8
	s_lshl_b32 s8, s39, 7
	s_add_u32 s10, s10, s8
	s_add_u32 s4, s4, s10
	s_addc_u32 s5, s5, 0
	s_lshl_b32 s14, s14, 19
	s_lshr_b32 s8, s39, 2
	s_lshl_b32 s8, s8, 18
	s_add_u32 s14, s14, s8
	s_and_b32 s8, s39, 3
	s_lshl_b32 s8, s8, 15
	s_add_u32 s14, s14, s8
	s_lshl_b32 s8, s11, 17
	s_add_u32 s14, s14, s8
	s_lshl_b32 s8, s38, 7
	s_add_u32 s14, s14, s8
	s_add_u32 s92, s84, s14
	s_addc_u32 s93, s85, 0
	s_movk_i32 s25, 0x400
	s_movk_i32 s27, 0x1000
	s_movk_i32 s8, 0x400
	s_movk_i32 s9, 0x4000
	s_branch .Lcv2_goA1
